# adds DPP wave prefix-scan (row_shr/row_bcast) replacing 7 serial ds_bpermute round trips in the DeltaNet gate computation
# speedup vs baseline: 1.0264x; 1.0016x over previous
.LBB0_229:
	s_or_b64 exec, exec, s[0:1]
	s_waitcnt vmcnt(36)
	v_mul_f32_e32 v25, 0x3fb8aa3b, v34
	v_exp_f32_e32 v25, v25
	v_and_b32_e32 v100, 64, v209
	v_mul_f32_e64 v54, v24, -v25
	v_readlane_b32 s0, v253, 41
	v_readlane_b32 s1, v253, 42
	s_ashr_i32 s77, s76, 31
	v_mov_b32_e32 v25, v54
	s_nop 1
	v_add_f32_dpp v25, v25, v25 row_shr:1 row_mask:0xf bank_mask:0xf
	s_nop 1
	v_add_f32_dpp v25, v25, v25 row_shr:2 row_mask:0xf bank_mask:0xf
	s_nop 1
	v_add_f32_dpp v25, v25, v25 row_shr:4 row_mask:0xf bank_mask:0xf
	s_nop 1
	v_add_f32_dpp v25, v25, v25 row_shr:8 row_mask:0xf bank_mask:0xf
	s_nop 1
	v_add_f32_dpp v25, v25, v25 row_bcast:15 row_mask:0xa bank_mask:0xf
	s_nop 1
	v_add_f32_dpp v25, v25, v25 row_bcast:31 row_mask:0xc bank_mask:0xf
	s_nop 1
	v_readlane_b32 s99, v25, 63
	s_nop 1
	v_mov_b32_e32 v24, s99
	v_mul_f32_e32 v34, 0x3fb8aa3b, v25
	v_exp_f32_e32 v94, v34
	s_andn2_b64 vcc, exec, s[0:1]
	s_cbranch_vccnz .LBB0_233
	s_waitcnt lgkmcnt(0)
	v_sub_f32_e32 v34, v24, v25
	v_mul_f32_e32 v34, 0x3fb8aa3b, v34
	v_exp_f32_e32 v34, v34
	v_lshl_add_u32 v54, v215, 2, 0
	v_add_u32_e32 v55, 0x1c400, v54
	ds_write_b32 v55, v25
	v_add_u32_e32 v25, 0x1c600, v54
	ds_write_b32 v25, v94
	v_add_u32_e32 v25, 0x1c700, v54
	v_cmp_eq_u32_e32 vcc, 0, v215
	ds_write_b32 v25, v34
	s_and_saveexec_b64 s[0:1], vcc
	s_cbranch_execz .LBB0_232
	s_lshl_b64 s[2:3], s[76:77], 2
	v_readlane_b32 s20, v253, 25
	s_add_u32 s2, s20, s2
	v_readlane_b32 s20, v253, 26
	s_addc_u32 s3, s20, s3
	global_store_dword v141, v24, s[2:3]
